# sel: K ds_reads issued right after the block-selected test (before the per-block scalar setup), threshold adds moved into the tile setup
# speedup vs baseline: 1.0344x; 1.0013x over previous
; __device__ __forceinline__ float xmax16(float v) { float a = v, b = v; PL_SWAP16(a, b); return fmaxf(a, b); }
; __device__ __forceinline__ float xmax32(float v) { float a = v, b = v; PL_SWAP32(a, b); return fmaxf(a, b); }
; __device__ __forceinline__ unsigned lds_addr(const LAS void* p) { return (unsigned)(size_t)p; }
; template <class G> __device__ __forceinline__ void online_sm8(f32x4 (&s)[4], G& g, const float ref) {
;     float mx = s[0][0];
; #pragma unroll
;     for (int T_ = 0; T_ < 4; ++T_)
; #pragma unroll
;         for (int i = 0; i < 4; ++i) mx = fmaxf(mx, s[T_][i]);
;     const float t = mx + (ref - 5.f);
;     if (!__all(t <= g.m + SM_THR8)) {
;         const float mr = xmax32(xmax16(t));
;         const float mn = fmaxf(g.m, mr); const float al = __builtin_amdgcn_exp2f(g.m - mn); g.m = mn; g.l *= al;
; #pragma unroll
;         for (int dt = 0; dt < 8; ++dt) g.o[dt] = g.o[dt] * al;
;         const float d = ref - mn;
; #pragma unroll
;         for (int T_ = 0; T_ < 4; ++T_)
; #pragma unroll
;             for (int i = 0; i < 4; ++i) s[T_][i] += d;
;     }
; template <bool DUMMY> __device__ __forceinline__ void sel_phase(Frame& F) {
;     ...
;                 unsigned byte = (cb >> (8 * h)) & 0xffu;
;                 if (DUMMY && MK_EXP == 1) byte = 0u;
;                 const unsigned a0 = byte & 0xfu, a1 = byte >> 4;
;                 if (byte == 0u) continue;
;                 const bool selA = ((a0 >> (c >> 2)) & 1u) != 0u, selB = ((a1 >> (c >> 2)) & 1u) != 0u;
;                 const float NINF = -__builtin_inff();
;                 const int kb = jc * 64; const bool diag = (jc == cur); f32x4 s0[4], s1[4];
;                 const float bA = selA ? 0.f : NINF, bB = selB ? 0.f : NINF;
;                 if (a0 != 0u) {
;                     const float rf = sm8_ref(g0);
;                     VT8Frag vf; qk8_tile_c(s0, g0, lds_addr(sb) + (unsigned)klane, bA + (5.f - rf)); pv8_issue(vf, lds_addr(sb + K8TB) + (unsigned)vtlane);
;                     if (diag) mask_scores(s0, tokA, 0x40000000u, kb, kq);
;                     online_sm8(s0, g0, rf);
.Lsel_nodma:
	s_lshr_b32 s45, s67, s36
	s_and_b32 s97, s45, 0xff
	s_cmp_eq_u32 s97, 0
	s_cbranch_scc1 .LBB0_1798
	ds_read_b128 v[84:87], v208 offset:0
	ds_read_b128 v[88:91], v208 offset:16
	ds_read_b128 v[92:95], v208 offset:0x900
	ds_read_b128 v[96:99], v208 offset:0x910
	ds_read_b128 v[118:121], v208 offset:0x1200
	ds_read_b128 v[122:125], v208 offset:0x1210
	ds_read_b128 v[126:129], v208 offset:0x1b00
	ds_read_b128 v[130:133], v208 offset:0x1b10
	s_lshr_b32 s12, s66, s36
	s_and_b32 s12, s12, 0xff
	s_lshl_b32 s44, s12, 6
	s_cmp_eq_u32 s12, s58
	s_cselect_b64 s[12:13], 0, -1
	s_and_b32 vcc_lo, s45, 15
	s_cbranch_scc0 .Lsel_g1_pre
	v_and_b32_e32 v18, s45, v154
	v_cmp_eq_u32_e32 vcc, 0, v18
	s_nop 1
	v_cndmask_b32_e32 v18, 0, v181, vcc
	v_cmp_ngt_f32_e32 vcc, s90, v19
	s_nop 1
	v_cndmask_b32_e32 v116, 0, v19, vcc
	v_add_f32_e32 v150, 0xc0a00000, v116
	v_add_f32_e32 v151, v19, v115
	v_sub_f32_e32 v114, 0x40a00000, v116
	v_add_f32_e32 v210, v114, v18
	v_mov_b32_e32 v211, v210
	v_mov_b32_e32 v212, v210
	v_mov_b32_e32 v213, v210
	s_waitcnt lgkmcnt(6)
	s_nop 1
	v_mfma_scale_f32_16x16x128_f8f6f4 v[84:87], v[84:91], v[0:7], v[210:213], v178, v177 op_sel_hi:[0,0,0]
	ds_read_b64 v[148:149], v207 offset:0
	ds_read_b64 v[146:147], v207 offset:32
	ds_read_b64 v[144:145], v207 offset:0x500
	ds_read_b64 v[142:143], v207 offset:0x520
	ds_read_b64 v[140:141], v207 offset:0xa00
	ds_read_b64 v[136:137], v207 offset:0xa20
	ds_read_b64 v[138:139], v207 offset:0xf00
	ds_read_b64 v[134:135], v207 offset:0xf20
	s_waitcnt lgkmcnt(12)
	v_mfma_scale_f32_16x16x128_f8f6f4 v[88:91], v[92:99], v[0:7], v[210:213], v178, v177 op_sel_hi:[0,0,0]
	s_waitcnt lgkmcnt(10)
	v_mfma_scale_f32_16x16x128_f8f6f4 v[92:95], v[118:125], v[0:7], v[210:213], v178, v177 op_sel_hi:[0,0,0]
	s_waitcnt lgkmcnt(8)
	v_mfma_scale_f32_16x16x128_f8f6f4 v[96:99], v[126:133], v[0:7], v[210:213], v178, v177 op_sel_hi:[0,0,0]
	ds_read_b64 v[132:133], v207 offset:0x1400
	ds_read_b64 v[130:131], v207 offset:0x1420
	ds_read_b64 v[128:129], v207 offset:0x1900
	ds_read_b64 v[126:127], v207 offset:0x1920
	ds_read_b64 v[124:125], v207 offset:0x1e00
	ds_read_b64 v[120:121], v207 offset:0x1e20
	ds_read_b64 v[118:119], v207 offset:0x2300
	ds_read_b64 v[122:123], v207 offset:0x2320
	s_and_b64 vcc, exec, s[12:13]
	s_cbranch_vccnz .LBB0_1806
	v_add_u32_e32 v18, s44, v155
	v_sub_u32_e32 v114, s55, v18
	v_cmp_gt_u32_e32 vcc, 2.0, v114
	v_sub_u32_e32 v114, v18, v16
	s_nop 2
	v_cndmask_b32_e32 v84, v181, v84, vcc
	v_cmp_lt_u32_e32 vcc, s91, v114
	v_sub_u32_e32 v114, v184, v18
	s_nop 0
	v_cndmask_b32_e32 v85, v181, v85, vcc
	v_cmp_gt_u32_e32 vcc, 2.0, v114
	v_sub_u32_e32 v114, v185, v18
	s_nop 0
	v_cndmask_b32_e32 v86, v181, v86, vcc
	v_cmp_gt_u32_e32 vcc, 2.0, v114
	v_sub_u32_e32 v114, s68, v18
	s_nop 0
	v_cndmask_b32_e32 v87, v181, v87, vcc
	v_cmp_gt_u32_e32 vcc, 2.0, v114
	v_sub_u32_e32 v114, v186, v18
	s_nop 0
	v_cndmask_b32_e32 v88, v181, v88, vcc
	v_cmp_gt_u32_e32 vcc, 2.0, v114
	v_sub_u32_e32 v114, v187, v18
	s_nop 0
	v_cndmask_b32_e32 v89, v181, v89, vcc
	v_cmp_gt_u32_e32 vcc, 2.0, v114
	v_sub_u32_e32 v114, v188, v18
	s_nop 0
	v_cndmask_b32_e32 v90, v181, v90, vcc
	v_cmp_gt_u32_e32 vcc, 2.0, v114
	v_sub_u32_e32 v114, s69, v18
	s_nop 0
	v_cndmask_b32_e32 v91, v181, v91, vcc
	v_cmp_gt_u32_e32 vcc, 2.0, v114
	v_sub_u32_e32 v114, v189, v18
	s_nop 0
	v_cndmask_b32_e32 v92, v181, v92, vcc
	v_cmp_gt_u32_e32 vcc, 2.0, v114
	v_sub_u32_e32 v114, v190, v18
	s_nop 0
	v_cndmask_b32_e32 v93, v181, v93, vcc
	v_cmp_gt_u32_e32 vcc, 2.0, v114
	v_sub_u32_e32 v114, v191, v18
	s_nop 0
	v_cndmask_b32_e32 v94, v181, v94, vcc
	v_cmp_gt_u32_e32 vcc, 2.0, v114
	v_sub_u32_e32 v114, s70, v18
	s_nop 0
	v_cndmask_b32_e32 v95, v181, v95, vcc
	v_cmp_gt_u32_e32 vcc, 2.0, v114
	v_sub_u32_e32 v114, v192, v18
	s_nop 0
	v_cndmask_b32_e32 v96, v181, v96, vcc
	v_cmp_gt_u32_e32 vcc, 2.0, v114
	v_sub_u32_e32 v114, v193, v18
	v_sub_u32_e32 v18, v194, v18
	v_cndmask_b32_e32 v97, v181, v97, vcc
	v_cmp_gt_u32_e32 vcc, 2.0, v114
	s_nop 1
	v_cndmask_b32_e32 v98, v181, v98, vcc
	v_cmp_gt_u32_e32 vcc, 2.0, v18
	s_nop 1
	v_cndmask_b32_e32 v99, v181, v99, vcc
.LBB0_1806:
	v_max_f32_e32 v18, v84, v85
	v_max3_f32 v18, v18, v86, v87
	v_max3_f32 v18, v18, v88, v89
	v_max3_f32 v18, v18, v90, v91
	v_max3_f32 v18, v18, v92, v93
	v_max3_f32 v18, v18, v94, v95
	v_max3_f32 v18, v18, v96, v97
	v_max3_f32 v114, v18, v98, v99
	v_add_f32_e32 v150, v150, v114
	v_cmp_le_f32_e32 vcc, v150, v151
	s_cmp_eq_u64 vcc, exec
	s_cbranch_scc1 .LBB0_1808
	v_mov_b32_e32 v18, v84
	v_mov_b32_e32 v84, v150
	s_nop 1
	v_permlane16_swap_b32 v84, v150
	v_mov_b32_e32 v151, v96
	v_max_f32_e32 v114, v150, v150
	v_max_f32_e32 v84, v84, v84
	v_max_f32_e32 v84, v84, v114
	v_mov_b32_e32 v114, v84
	s_nop 1
	v_permlane32_swap_b32 v114, v84
	v_mov_b32_e32 v150, v92
	v_max3_f32 v114, v19, v114, v84
	v_sub_f32_e32 v19, v19, v114
	v_exp_f32_e32 v84, v19
	v_mov_b32_e32 v19, v88
	v_mov_b32_e32 v210, v85
	v_mov_b32_e32 v211, v86
	v_mul_f32_e32 v183, v183, v84
	v_pk_mul_f32 v[82:83], v[82:83], v[84:85] op_sel_hi:[1,0]
	v_pk_mul_f32 v[80:81], v[80:81], v[84:85] op_sel_hi:[1,0]
	v_pk_mul_f32 v[78:79], v[78:79], v[84:85] op_sel_hi:[1,0]
	v_pk_mul_f32 v[76:77], v[76:77], v[84:85] op_sel_hi:[1,0]
	v_pk_mul_f32 v[74:75], v[74:75], v[84:85] op_sel_hi:[1,0]
	v_pk_mul_f32 v[72:73], v[72:73], v[84:85] op_sel_hi:[1,0]
	v_pk_mul_f32 v[70:71], v[70:71], v[84:85] op_sel_hi:[1,0]
	v_pk_mul_f32 v[68:69], v[68:69], v[84:85] op_sel_hi:[1,0]
	v_pk_mul_f32 v[66:67], v[66:67], v[84:85] op_sel_hi:[1,0]
	v_pk_mul_f32 v[64:65], v[64:65], v[84:85] op_sel_hi:[1,0]
	v_pk_mul_f32 v[62:63], v[62:63], v[84:85] op_sel_hi:[1,0]
	v_pk_mul_f32 v[60:61], v[60:61], v[84:85] op_sel_hi:[1,0]
	v_pk_mul_f32 v[58:59], v[58:59], v[84:85] op_sel_hi:[1,0]
	v_pk_mul_f32 v[56:57], v[56:57], v[84:85] op_sel_hi:[1,0]
	v_pk_mul_f32 v[54:55], v[54:55], v[84:85] op_sel_hi:[1,0]
	v_pk_mul_f32 v[52:53], v[52:53], v[84:85] op_sel_hi:[1,0]
	v_sub_f32_e32 v84, v116, v114
	v_pk_add_f32 v[212:213], v[18:19], v[84:85] op_sel_hi:[1,0]
	v_mov_b32_e32 v18, v89
	v_mov_b32_e32 v19, v90
	v_pk_add_f32 v[214:215], v[18:19], v[84:85] op_sel_hi:[1,0]
	v_mov_b32_e32 v18, v93
	v_mov_b32_e32 v19, v94
	v_pk_add_f32 v[88:89], v[18:19], v[84:85] op_sel_hi:[1,0]
	v_mov_b32_e32 v18, v97
	v_mov_b32_e32 v19, v98
	v_pk_add_f32 v[210:211], v[210:211], v[84:85] op_sel_hi:[1,0]
	v_pk_add_f32 v[150:151], v[150:151], v[84:85] op_sel_hi:[1,0]
	v_pk_add_f32 v[92:93], v[18:19], v[84:85] op_sel_hi:[1,0]
	v_add_f32_e32 v87, v87, v84
	v_add_f32_e32 v91, v91, v84
	v_add_f32_e32 v95, v95, v84
	v_add_f32_e32 v99, v99, v84
	v_mov_b32_e32 v19, v114
	v_mov_b32_e32 v97, v92
	v_mov_b32_e32 v98, v93
	v_mov_b32_e32 v93, v88
	v_mov_b32_e32 v94, v89
	v_mov_b32_e32 v89, v214
	v_mov_b32_e32 v90, v215
	v_mov_b32_e32 v85, v210
	v_mov_b32_e32 v86, v211
	v_mov_b32_e32 v84, v212
	v_mov_b32_e32 v88, v213
	v_mov_b32_e32 v92, v150
	v_mov_b32_e32 v96, v151

; __device__ __forceinline__ float xmax16(float v) { float a = v, b = v; PL_SWAP16(a, b); return fmaxf(a, b); }
; __device__ __forceinline__ float xmax32(float v) { float a = v, b = v; PL_SWAP32(a, b); return fmaxf(a, b); }
; __device__ __forceinline__ unsigned lds_addr(const LAS void* p) { return (unsigned)(size_t)p; }
; template <class G> __device__ __forceinline__ void online_sm8(f32x4 (&s)[4], G& g, const float ref) {
;     float mx = s[0][0];
; #pragma unroll
;     for (int T_ = 0; T_ < 4; ++T_)
; #pragma unroll
;         for (int i = 0; i < 4; ++i) mx = fmaxf(mx, s[T_][i]);
;     const float t = mx + (ref - 5.f);
;     if (!__all(t <= g.m + SM_THR8)) {
;         const float mr = xmax32(xmax16(t));
;         const float mn = fmaxf(g.m, mr); const float al = __builtin_amdgcn_exp2f(g.m - mn); g.m = mn; g.l *= al;
; #pragma unroll
;         for (int dt = 0; dt < 8; ++dt) g.o[dt] = g.o[dt] * al;
;         const float d = ref - mn;
; #pragma unroll
;         for (int T_ = 0; T_ < 4; ++T_)
; #pragma unroll
;             for (int i = 0; i < 4; ++i) s[T_][i] += d;
;     }
; template <bool DUMMY> __device__ __forceinline__ void sel_phase(Frame& F) {
;     ...
;                 if (a1 != 0u) {
;                     const float rf = sm8_ref(g1);
;                     VT8Frag vf; qk8_tile_c(s0, g1, lds_addr(sb) + (unsigned)klane, bB + (5.f - rf)); pv8_issue(vf, lds_addr(sb + K8TB) + (unsigned)vtlane);
;                     if (diag) mask_scores(s0, tokA + 4, 0x40000000u, kb, kq);
;                     online_sm8(s0, g1, rf);
;                     pv8_mm(g1, s0, vf);
.LBB0_1809:
	s_cmp_lt_u32 s97, 16
	s_cbranch_scc1 .LBB0_1798
	ds_read_b128 v[84:87], v208 offset:0
	ds_read_b128 v[88:91], v208 offset:16
	ds_read_b128 v[92:95], v208 offset:0x900
	ds_read_b128 v[96:99], v208 offset:0x910
	ds_read_b128 v[118:121], v208 offset:0x1200
	ds_read_b128 v[122:125], v208 offset:0x1210
	ds_read_b128 v[126:129], v208 offset:0x1b00
	ds_read_b128 v[130:133], v208 offset:0x1b10
.Lsel_g1_pre:
	s_lshr_b32 s45, s45, 4
	v_and_b32_e32 v18, s45, v154
	v_cmp_eq_u32_e32 vcc, 0, v18
	s_nop 1
	v_cndmask_b32_e32 v114, 0, v181, vcc
	v_cmp_ngt_f32_e32 vcc, s90, v117
	s_nop 1
	v_cndmask_b32_e32 v18, 0, v117, vcc
	v_add_f32_e32 v150, 0xc0a00000, v18
	v_add_f32_e32 v151, v117, v115
	v_sub_f32_e32 v116, 0x40a00000, v18
	v_add_f32_e32 v210, v114, v116
	v_mov_b32_e32 v211, v210
	v_mov_b32_e32 v212, v210
	v_mov_b32_e32 v213, v210
	s_waitcnt lgkmcnt(6)
	s_nop 1
	v_mfma_scale_f32_16x16x128_f8f6f4 v[84:87], v[84:91], v[8:15], v[210:213], v178, v177 op_sel_hi:[0,0,0]
	ds_read_b64 v[148:149], v207 offset:0
	ds_read_b64 v[146:147], v207 offset:32
	ds_read_b64 v[144:145], v207 offset:0x500
	ds_read_b64 v[142:143], v207 offset:0x520
	ds_read_b64 v[140:141], v207 offset:0xa00
	ds_read_b64 v[136:137], v207 offset:0xa20
	ds_read_b64 v[138:139], v207 offset:0xf00
	ds_read_b64 v[134:135], v207 offset:0xf20
	s_waitcnt lgkmcnt(12)
	v_mfma_scale_f32_16x16x128_f8f6f4 v[88:91], v[92:99], v[8:15], v[210:213], v178, v177 op_sel_hi:[0,0,0]
	s_waitcnt lgkmcnt(10)
	v_mfma_scale_f32_16x16x128_f8f6f4 v[92:95], v[118:125], v[8:15], v[210:213], v178, v177 op_sel_hi:[0,0,0]
	s_waitcnt lgkmcnt(8)
	v_mfma_scale_f32_16x16x128_f8f6f4 v[96:99], v[126:133], v[8:15], v[210:213], v178, v177 op_sel_hi:[0,0,0]
	ds_read_b64 v[132:133], v207 offset:0x1400
	ds_read_b64 v[130:131], v207 offset:0x1420
	ds_read_b64 v[128:129], v207 offset:0x1900
	ds_read_b64 v[126:127], v207 offset:0x1920
	ds_read_b64 v[124:125], v207 offset:0x1e00
	ds_read_b64 v[120:121], v207 offset:0x1e20
	ds_read_b64 v[118:119], v207 offset:0x2300
	ds_read_b64 v[122:123], v207 offset:0x2320
	s_and_b64 vcc, exec, s[12:13]
	s_cbranch_vccnz .LBB0_1812
	v_add_u32_e32 v114, s44, v155
	v_sub_u32_e32 v116, v195, v114
	v_cmp_gt_u32_e32 vcc, 2.0, v116
	v_sub_u32_e32 v116, v114, v195
	s_nop 2
	v_cndmask_b32_e32 v84, v181, v84, vcc
	v_cmp_lt_u32_e32 vcc, s91, v116
	v_sub_u32_e32 v116, v196, v114
	s_nop 0
	v_cndmask_b32_e32 v85, v181, v85, vcc
	v_cmp_gt_u32_e32 vcc, 2.0, v116
	v_sub_u32_e32 v116, v197, v114
	s_nop 0
	v_cndmask_b32_e32 v86, v181, v86, vcc
	v_cmp_gt_u32_e32 vcc, 2.0, v116
	v_sub_u32_e32 v116, s71, v114
	s_nop 0
	v_cndmask_b32_e32 v87, v181, v87, vcc
	v_cmp_gt_u32_e32 vcc, 2.0, v116
	v_sub_u32_e32 v116, v198, v114
	s_nop 0
	v_cndmask_b32_e32 v88, v181, v88, vcc
	v_cmp_gt_u32_e32 vcc, 2.0, v116
	v_sub_u32_e32 v116, v199, v114
	s_nop 0
	v_cndmask_b32_e32 v89, v181, v89, vcc
	v_cmp_gt_u32_e32 vcc, 2.0, v116
	v_sub_u32_e32 v116, v200, v114
	s_nop 0
	v_cndmask_b32_e32 v90, v181, v90, vcc
	v_cmp_gt_u32_e32 vcc, 2.0, v116
	v_sub_u32_e32 v116, s72, v114
	s_nop 0
	v_cndmask_b32_e32 v91, v181, v91, vcc
	v_cmp_gt_u32_e32 vcc, 2.0, v116
	v_sub_u32_e32 v116, v201, v114
	s_nop 0
	v_cndmask_b32_e32 v92, v181, v92, vcc
	v_cmp_gt_u32_e32 vcc, 2.0, v116
	v_sub_u32_e32 v116, v202, v114
	s_nop 0
	v_cndmask_b32_e32 v93, v181, v93, vcc
	v_cmp_gt_u32_e32 vcc, 2.0, v116
	v_sub_u32_e32 v116, v203, v114
	s_nop 0
	v_cndmask_b32_e32 v94, v181, v94, vcc
	v_cmp_gt_u32_e32 vcc, 2.0, v116
	v_sub_u32_e32 v116, s73, v114
	s_nop 0
	v_cndmask_b32_e32 v95, v181, v95, vcc
	v_cmp_gt_u32_e32 vcc, 2.0, v116
	v_sub_u32_e32 v116, v204, v114
	s_nop 0
	v_cndmask_b32_e32 v96, v181, v96, vcc
	v_cmp_gt_u32_e32 vcc, 2.0, v116
	v_sub_u32_e32 v116, v205, v114
	v_sub_u32_e32 v114, v206, v114
	v_cndmask_b32_e32 v97, v181, v97, vcc
	v_cmp_gt_u32_e32 vcc, 2.0, v116
	s_nop 1
	v_cndmask_b32_e32 v98, v181, v98, vcc
	v_cmp_gt_u32_e32 vcc, 2.0, v114
	s_nop 1
	v_cndmask_b32_e32 v99, v181, v99, vcc
.LBB0_1812:
	v_max_f32_e32 v114, v84, v85
	v_max3_f32 v114, v114, v86, v87
	v_max3_f32 v114, v114, v88, v89
	v_max3_f32 v114, v114, v90, v91
	v_max3_f32 v114, v114, v92, v93
	v_max3_f32 v114, v114, v94, v95
	v_max3_f32 v114, v114, v96, v97
	v_max3_f32 v114, v114, v98, v99
	v_add_f32_e32 v150, v150, v114
	v_cmp_le_f32_e32 vcc, v150, v151
	s_cmp_eq_u64 vcc, exec
	s_cbranch_scc1 .LBB0_1797
	v_mov_b32_e32 v116, v84
	v_mov_b32_e32 v84, v150
	s_nop 1
	v_permlane16_swap_b32 v150, v84
	v_mov_b32_e32 v151, v96
	v_max_f32_e32 v84, v84, v84
	v_max_f32_e32 v114, v150, v150
	v_max_f32_e32 v84, v114, v84
	v_mov_b32_e32 v114, v84
	s_nop 1
	v_permlane32_swap_b32 v84, v114
	v_mov_b32_e32 v150, v92
	v_max3_f32 v114, v117, v84, v114
	v_sub_f32_e32 v84, v117, v114
	v_exp_f32_e32 v84, v84
	v_sub_f32_e32 v18, v18, v114
	v_mov_b32_e32 v117, v88
	v_mov_b32_e32 v88, v93
	v_mul_f32_e32 v182, v182, v84
	v_pk_mul_f32 v[50:51], v[50:51], v[84:85] op_sel_hi:[1,0]
	v_pk_mul_f32 v[48:49], v[48:49], v[84:85] op_sel_hi:[1,0]
	v_pk_mul_f32 v[46:47], v[46:47], v[84:85] op_sel_hi:[1,0]
	v_pk_mul_f32 v[44:45], v[44:45], v[84:85] op_sel_hi:[1,0]
	v_pk_mul_f32 v[42:43], v[42:43], v[84:85] op_sel_hi:[1,0]
	v_pk_mul_f32 v[40:41], v[40:41], v[84:85] op_sel_hi:[1,0]
	v_pk_mul_f32 v[38:39], v[38:39], v[84:85] op_sel_hi:[1,0]
	v_pk_mul_f32 v[36:37], v[36:37], v[84:85] op_sel_hi:[1,0]
	v_pk_mul_f32 v[34:35], v[34:35], v[84:85] op_sel_hi:[1,0]
	v_pk_mul_f32 v[32:33], v[32:33], v[84:85] op_sel_hi:[1,0]
	v_pk_mul_f32 v[30:31], v[30:31], v[84:85] op_sel_hi:[1,0]
	v_pk_mul_f32 v[28:29], v[28:29], v[84:85] op_sel_hi:[1,0]
	v_pk_mul_f32 v[26:27], v[26:27], v[84:85] op_sel_hi:[1,0]
	v_pk_mul_f32 v[24:25], v[24:25], v[84:85] op_sel_hi:[1,0]
	v_pk_mul_f32 v[22:23], v[22:23], v[84:85] op_sel_hi:[1,0]
	v_pk_mul_f32 v[20:21], v[20:21], v[84:85] op_sel_hi:[1,0]
	v_mov_b32_e32 v84, v85
	v_mov_b32_e32 v85, v86
	v_pk_add_f32 v[210:211], v[84:85], v[18:19] op_sel_hi:[1,0]
	v_mov_b32_e32 v84, v89
	v_mov_b32_e32 v85, v90
	v_mov_b32_e32 v89, v94
	v_mov_b32_e32 v92, v97
	v_mov_b32_e32 v93, v98
	v_pk_add_f32 v[212:213], v[116:117], v[18:19] op_sel_hi:[1,0]
	v_pk_add_f32 v[84:85], v[84:85], v[18:19] op_sel_hi:[1,0]
	v_pk_add_f32 v[88:89], v[88:89], v[18:19] op_sel_hi:[1,0]
	v_pk_add_f32 v[150:151], v[150:151], v[18:19] op_sel_hi:[1,0]
	v_pk_add_f32 v[92:93], v[92:93], v[18:19] op_sel_hi:[1,0]
	v_add_f32_e32 v87, v87, v18
	v_add_f32_e32 v91, v91, v18
	v_add_f32_e32 v95, v95, v18
	v_add_f32_e32 v99, v99, v18
	v_mov_b32_e32 v117, v114
	v_mov_b32_e32 v97, v92
	v_mov_b32_e32 v98, v93
	v_mov_b32_e32 v93, v88
	v_mov_b32_e32 v94, v89
	v_mov_b32_e32 v89, v84
	v_mov_b32_e32 v90, v85
	v_mov_b32_e32 v85, v210
	v_mov_b32_e32 v86, v211
	v_mov_b32_e32 v84, v212
	v_mov_b32_e32 v88, v213
	v_mov_b32_e32 v92, v150
	v_mov_b32_e32 v96, v151
	s_branch .LBB0_1797
